# speedup vs baseline: 1.0120x; 1.0120x over previous
.LBB0_20:
	s_or_b64 exec, exec, s[8:9]
	s_movk_i32 s8, 0x1df
	v_cmp_gt_u32_e64 s[8:9], s8, v0
	v_mov_b32_e32 v53, 0
	s_barrier
	s_and_saveexec_b64 s[10:11], s[8:9]
	ds_read_b32 v53, v1 offset:50000
	s_or_b64 exec, exec, s[10:11]
	s_waitcnt lgkmcnt(0)
	v_mov_b32_e32 v54, v53
	s_nop 1
	v_add_u32_dpp v54, v54, v54 row_shr:1 row_mask:0xf bank_mask:0xf bound_ctrl:0
	s_nop 1
	v_add_u32_dpp v54, v54, v54 row_shr:2 row_mask:0xf bank_mask:0xf bound_ctrl:0
	s_nop 1
	v_add_u32_dpp v54, v54, v54 row_shr:4 row_mask:0xf bank_mask:0xf bound_ctrl:0
	s_nop 1
	v_add_u32_dpp v54, v54, v54 row_shr:8 row_mask:0xf bank_mask:0xf bound_ctrl:0
	s_nop 1
	v_add_u32_dpp v54, v54, v54 row_bcast:15 row_mask:0xa bank_mask:0xf
	s_nop 1
	v_add_u32_dpp v54, v54, v54 row_bcast:31 row_mask:0xc bank_mask:0xf
	v_cmp_eq_u32_e64 s[10:11], 63, v36
	s_and_saveexec_b64 s[12:13], s[10:11]
	v_lshlrev_b32_e32 v36, 2, v35
	ds_write_b32 v36, v54 offset:53840
	s_or_b64 exec, exec, s[12:13]
	s_load_dwordx2 s[12:13], s[0:1], 0x10
	s_load_dwordx2 s[10:11], s[0:1], 0x20
	v_cmp_lt_u32_e64 s[0:1], 63, v0
	v_mov_b32_e32 v36, 0
	s_waitcnt lgkmcnt(0)
	s_barrier
	s_and_saveexec_b64 s[14:15], s[0:1]
	s_cbranch_execz .LBB0_34
	v_readfirstlane_b32 s23, v35
	v_mov_b32_e32 v55, 0xd250
	ds_read_b128 v[56:59], v55
	ds_read_b128 v[60:63], v55 offset:16
	v_mov_b32_e32 v36, 0
	s_waitcnt lgkmcnt(0)
	v_add_u32_e32 v36, v36, v56
	s_cmp_eq_u32 s23, 1
	s_cbranch_scc1 .Lpp_done
	v_add_u32_e32 v36, v36, v57
	s_cmp_eq_u32 s23, 2
	s_cbranch_scc1 .Lpp_done
	v_add_u32_e32 v36, v36, v58
	s_cmp_eq_u32 s23, 3
	s_cbranch_scc1 .Lpp_done
	v_add_u32_e32 v36, v36, v59
	s_cmp_eq_u32 s23, 4
	s_cbranch_scc1 .Lpp_done
	v_add_u32_e32 v36, v36, v60
	s_cmp_eq_u32 s23, 5
	s_cbranch_scc1 .Lpp_done
	v_add_u32_e32 v36, v36, v61
	s_cmp_eq_u32 s23, 6
	s_cbranch_scc1 .Lpp_done
	v_add_u32_e32 v36, v36, v62
	s_cmp_eq_u32 s23, 7
	s_cbranch_scc1 .Lpp_done
	v_add_u32_e32 v36, v36, v63
	s_cmp_eq_u32 s23, 8
	s_cbranch_scc1 .Lpp_done
	ds_read_b128 v[56:59], v55 offset:32
	ds_read_b128 v[60:63], v55 offset:48
	s_waitcnt lgkmcnt(0)
	v_add_u32_e32 v36, v36, v56
	s_cmp_eq_u32 s23, 9
	s_cbranch_scc1 .Lpp_done
	v_add_u32_e32 v36, v36, v57
	s_cmp_eq_u32 s23, 10
	s_cbranch_scc1 .Lpp_done
	v_add_u32_e32 v36, v36, v58
	s_cmp_eq_u32 s23, 11
	s_cbranch_scc1 .Lpp_done
	v_add_u32_e32 v36, v36, v59
	s_cmp_eq_u32 s23, 12
	s_cbranch_scc1 .Lpp_done
	v_add_u32_e32 v36, v36, v60
	s_cmp_eq_u32 s23, 13
	s_cbranch_scc1 .Lpp_done
	v_add_u32_e32 v36, v36, v61
	s_cmp_eq_u32 s23, 14
	s_cbranch_scc1 .Lpp_done
	v_add_u32_e32 v36, v36, v62
.Lpp_done:
.LBB0_34:
	s_or_b64 exec, exec, s[14:15]
	s_and_saveexec_b64 s[0:1], s[8:9]
	s_cbranch_execz .LBB0_36
	v_sub_u32_e32 v35, v54, v53
	v_add_u32_e32 v35, v35, v36
	v_lshl_add_u32 v54, v0, 8, s22
	v_mov_b32_e32 v55, 0
	ds_write_b32 v1, v35 offset:51920
	v_lshl_or_b32 v1, v35, 16, v53
	v_lshl_add_u64 v[54:55], v[54:55], 2, s[12:13]
	global_store_dword v[54:55], v1, off

.LBB1_63:
	v_lshrrev_b32_e32 v25, 6, v0
	v_mov_b32_e32 v30, 0
	v_mov_b32_e32 v31, 0
	v_mov_b32_e32 v29, 0
	s_waitcnt lgkmcnt(0)
	s_barrier
	s_and_saveexec_b64 s[44:45], s[30:31]
	s_cbranch_execz .LBB1_67
	v_lshlrev_b32_e32 v12, 2, v0
	ds_read_b32 v29, v12 offset:34816
	v_and_b32_e32 v15, 63, v0
	s_waitcnt lgkmcnt(0)
	v_mov_b32_e32 v31, v29
	s_nop 1
	v_add_u32_dpp v31, v31, v31 row_shr:1 row_mask:0xf bank_mask:0xf bound_ctrl:0
	s_nop 1
	v_add_u32_dpp v31, v31, v31 row_shr:2 row_mask:0xf bank_mask:0xf bound_ctrl:0
	s_nop 1
	v_add_u32_dpp v31, v31, v31 row_shr:4 row_mask:0xf bank_mask:0xf bound_ctrl:0
	s_nop 1
	v_add_u32_dpp v31, v31, v31 row_shr:8 row_mask:0xf bank_mask:0xf bound_ctrl:0
	s_nop 1
	v_add_u32_dpp v31, v31, v31 row_bcast:15 row_mask:0xa bank_mask:0xf
	s_nop 1
	v_add_u32_dpp v31, v31, v31 row_bcast:31 row_mask:0xc bank_mask:0xf
	v_cmp_eq_u32_e32 vcc, 63, v15
	s_and_saveexec_b64 s[46:47], vcc
	v_lshlrev_b32_e32 v12, 2, v25
	ds_write_b32 v12, v31 offset:38912
	s_or_b64 exec, exec, s[46:47]
.LBB1_67:
	s_or_b64 exec, exec, s[44:45]
	s_load_dwordx2 s[52:53], s[0:1], 0x48
	s_load_dwordx2 s[56:57], s[0:1], 0x18
	s_load_dwordx2 s[54:55], s[0:1], 0x30
	s_waitcnt lgkmcnt(0)
	s_barrier
	ds_read_b128 v[12:15], v30 offset:38912
	s_and_saveexec_b64 s[44:45], s[30:31]
	s_cbranch_execz .LBB1_78
	v_cmp_lt_u32_e32 vcc, 63, v0
	v_mov_b32_e32 v30, 0
	s_and_saveexec_b64 s[30:31], vcc
	s_cbranch_execz .LBB1_72
	s_waitcnt lgkmcnt(0)
	v_mov_b32_e32 v30, v12
	v_cmp_lt_u32_e32 vcc, 1, v25
	s_nop 1
	v_cndmask_b32_e32 v32, 0, v13, vcc
	v_add_u32_e32 v30, v30, v32
	v_cmp_lt_u32_e32 vcc, 2, v25
	s_nop 1
	v_cndmask_b32_e32 v32, 0, v14, vcc
	v_add_u32_e32 v30, v30, v32
